# v8_vnop0_tail
# speedup vs baseline: 1.0216x; 1.0216x over previous
.Lchunk_loop:
	v_mfma_f32_16x16x32_f16 v[38:41], v[2:5], v[34:37], v[46:49]
	v_mfma_f32_16x16x32_f16 v[42:45], v[14:17], v[34:37], v[50:53]
	ds_read_b128 v[82:85], v94 offset:256
	ds_read_b128 v[86:89], v94 offset:272
	v_mfma_f32_16x16x32_f16 v[62:65], v[6:9], v[78:81], v[26:29]
	v_min_u32_e32 v1, v38, v40
	v_min_u32_e32 v0, v39, v41
	v_mfma_f32_16x16x32_f16 v[66:69], v[18:21], v[78:81], v[30:33]
	v_min3_u32 v1, v1, v42, v44
	v_min3_u32 v0, v0, v43, v45
	v_exp_f32_e32 v1, v1
	v_exp_f32_e32 v0, v0
	v_add_f32_e32 v1, 1.0, v1
	v_add_f32_e32 v0, 1.0, v0
	v_rcp_f32_e32 v1, v1
	v_rcp_f32_e32 v0, v0
	s_add_i32 s13, s8, 1
	v_cvt_pk_f16_f32 v34, v1, v0
	s_and_b32 s13, s13, 3
	s_mulk_i32 s13, 0x1100
	v_mov_b32_dpp v35, v34 quad_perm:[1,2,3,0] row_mask:0xf bank_mask:0xf bound_ctrl:1
	v_mov_b32_dpp v36, v34 quad_perm:[2,3,0,1] row_mask:0xf bank_mask:0xf bound_ctrl:1
	v_mov_b32_dpp v37, v34 quad_perm:[3,0,1,2] row_mask:0xf bank_mask:0xf bound_ctrl:1
	v_add_u32_e32 v95, s13, v177
	s_nop 0
	v_mfma_f32_16x16x32_f16 v[38:41], v[2:5], v[34:37], v[54:57]
	v_mfma_f32_16x16x32_f16 v[42:45], v[14:17], v[34:37], v[58:61]
	s_waitcnt lgkmcnt(0)
	v_mfma_f32_16x16x32_f16 v[70:73], v[10:13], v[78:81], v[26:29]
	v_min_u32_e32 v1, v38, v40
	v_min_u32_e32 v0, v39, v41
	v_mfma_f32_16x16x32_f16 v[74:77], v[22:25], v[78:81], v[30:33]
	v_min3_u32 v1, v1, v42, v44
	v_min3_u32 v0, v0, v43, v45
	v_exp_f32_e32 v1, v1
	v_exp_f32_e32 v0, v0
	v_add_f32_e32 v1, 1.0, v1
	v_add_f32_e32 v0, 1.0, v0
	v_rcp_f32_e32 v1, v1
	v_rcp_f32_e32 v0, v0
	v_cvt_pk_f16_f32 v78, v82, v83
	v_cvt_pk_f16_f32 v34, v1, v0
	v_cvt_pk_f16_f32 v79, v84, v85
	v_cvt_pk_f16_f32 v80, v86, v87
	v_mov_b32_dpp v35, v34 quad_perm:[1,2,3,0] row_mask:0xf bank_mask:0xf bound_ctrl:1
	v_mov_b32_dpp v36, v34 quad_perm:[2,3,0,1] row_mask:0xf bank_mask:0xf bound_ctrl:1
	v_mov_b32_dpp v37, v34 quad_perm:[3,0,1,2] row_mask:0xf bank_mask:0xf bound_ctrl:1
	v_cvt_pk_f16_f32 v81, v88, v89
	s_nop 0
	v_mfma_f32_16x16x32_f16 v[38:41], v[2:5], v[34:37], v[62:65]
	v_mfma_f32_16x16x32_f16 v[42:45], v[14:17], v[34:37], v[66:69]
	ds_read_b128 v[82:85], v94 offset:384
	ds_read_b128 v[86:89], v94 offset:400
	v_mfma_f32_16x16x32_f16 v[46:49], v[6:9], v[78:81], v[26:29]
	v_min_u32_e32 v1, v38, v40
	v_min_u32_e32 v0, v39, v41
	v_mfma_f32_16x16x32_f16 v[50:53], v[18:21], v[78:81], v[30:33]
	v_min3_u32 v1, v1, v42, v44
	v_min3_u32 v0, v0, v43, v45
	v_exp_f32_e32 v1, v1
	v_exp_f32_e32 v0, v0
	v_add_f32_e32 v1, 1.0, v1
	v_add_f32_e32 v0, 1.0, v0
	v_rcp_f32_e32 v1, v1
	v_rcp_f32_e32 v0, v0
	s_and_b32 s9, s8, 3
	v_cvt_pk_f16_f32 v34, v1, v0
	s_mulk_i32 s9, 0x1100
	s_add_i32 s9, s9, s24
	v_mov_b32_dpp v35, v34 quad_perm:[1,2,3,0] row_mask:0xf bank_mask:0xf bound_ctrl:1
	v_mov_b32_dpp v36, v34 quad_perm:[2,3,0,1] row_mask:0xf bank_mask:0xf bound_ctrl:1
	v_mov_b32_dpp v37, v34 quad_perm:[3,0,1,2] row_mask:0xf bank_mask:0xf bound_ctrl:1
	s_min_u32 s12, s8, 27
	s_lshl_b32 s22, s12, 10
	v_mfma_f32_16x16x32_f16 v[38:41], v[2:5], v[34:37], v[70:73]
	v_mfma_f32_16x16x32_f16 v[42:45], v[14:17], v[34:37], v[74:77]
	s_waitcnt lgkmcnt(0)
	v_mfma_f32_16x16x32_f16 v[54:57], v[10:13], v[78:81], v[26:29]
	v_min_u32_e32 v1, v38, v40
	v_min_u32_e32 v0, v39, v41
	v_mfma_f32_16x16x32_f16 v[58:61], v[22:25], v[78:81], v[30:33]
	v_min3_u32 v1, v1, v42, v44
	v_min3_u32 v0, v0, v43, v45
	v_exp_f32_e32 v1, v1
	v_exp_f32_e32 v0, v0
	v_add_f32_e32 v1, 1.0, v1
	v_add_f32_e32 v0, 1.0, v0
	v_rcp_f32_e32 v1, v1
	v_rcp_f32_e32 v0, v0
	v_cvt_pk_f16_f32 v78, v82, v83
	v_cvt_pk_f16_f32 v34, v1, v0
	v_cvt_pk_f16_f32 v79, v84, v85
	v_cvt_pk_f16_f32 v80, v86, v87
	v_mov_b32_dpp v35, v34 quad_perm:[1,2,3,0] row_mask:0xf bank_mask:0xf bound_ctrl:1
	v_mov_b32_dpp v36, v34 quad_perm:[2,3,0,1] row_mask:0xf bank_mask:0xf bound_ctrl:1
	v_mov_b32_dpp v37, v34 quad_perm:[3,0,1,2] row_mask:0xf bank_mask:0xf bound_ctrl:1
	v_cvt_pk_f16_f32 v81, v88, v89
	s_cmp_lt_u32 s8, 28
	s_cselect_b64 vcc, -1, 0
	v_mfma_f32_16x16x32_f16 v[38:41], v[2:5], v[34:37], v[46:49]
	v_mfma_f32_16x16x32_f16 v[42:45], v[14:17], v[34:37], v[50:53]
	ds_read_b128 v[82:85], v94 offset:512
	ds_read_b128 v[86:89], v94 offset:528
	v_mfma_f32_16x16x32_f16 v[62:65], v[6:9], v[78:81], v[26:29]
	v_min_u32_e32 v1, v38, v40
	v_min_u32_e32 v0, v39, v41
	v_mfma_f32_16x16x32_f16 v[66:69], v[18:21], v[78:81], v[30:33]
	v_min3_u32 v1, v1, v42, v44
	v_min3_u32 v0, v0, v43, v45
	v_exp_f32_e32 v1, v1
	v_exp_f32_e32 v0, v0
	v_add_f32_e32 v1, 1.0, v1
	v_add_f32_e32 v0, 1.0, v0
	v_rcp_f32_e32 v1, v1
	v_rcp_f32_e32 v0, v0
	v_lshl_add_u64 v[90:91], v[166:167], 0, s[22:23]
	v_cvt_pk_f16_f32 v34, v1, v0
	s_add_i32 s8, s8, 1
	s_nop 0
	v_mov_b32_dpp v35, v34 quad_perm:[1,2,3,0] row_mask:0xf bank_mask:0xf bound_ctrl:1
	v_mov_b32_dpp v36, v34 quad_perm:[2,3,0,1] row_mask:0xf bank_mask:0xf bound_ctrl:1
	v_mov_b32_dpp v37, v34 quad_perm:[3,0,1,2] row_mask:0xf bank_mask:0xf bound_ctrl:1
	s_nop 0
	s_nop 0
	v_mfma_f32_16x16x32_f16 v[38:41], v[2:5], v[34:37], v[54:57]
	v_mfma_f32_16x16x32_f16 v[42:45], v[14:17], v[34:37], v[58:61]
	s_waitcnt lgkmcnt(0)
	v_mfma_f32_16x16x32_f16 v[70:73], v[10:13], v[78:81], v[26:29]
	v_min_u32_e32 v1, v38, v40
	v_min_u32_e32 v0, v39, v41
	v_mfma_f32_16x16x32_f16 v[74:77], v[22:25], v[78:81], v[30:33]
	v_min3_u32 v1, v1, v42, v44
	v_min3_u32 v0, v0, v43, v45
	v_exp_f32_e32 v1, v1
	v_exp_f32_e32 v0, v0
	v_add_f32_e32 v1, 1.0, v1
	v_add_f32_e32 v0, 1.0, v0
	v_rcp_f32_e32 v1, v1
	v_rcp_f32_e32 v0, v0
	v_cvt_pk_f16_f32 v78, v82, v83
	v_cvt_pk_f16_f32 v34, v1, v0
	v_cvt_pk_f16_f32 v79, v84, v85
	v_cvt_pk_f16_f32 v80, v86, v87
	v_mov_b32_dpp v35, v34 quad_perm:[1,2,3,0] row_mask:0xf bank_mask:0xf bound_ctrl:1
	v_mov_b32_dpp v36, v34 quad_perm:[2,3,0,1] row_mask:0xf bank_mask:0xf bound_ctrl:1
	v_mov_b32_dpp v37, v34 quad_perm:[3,0,1,2] row_mask:0xf bank_mask:0xf bound_ctrl:1
	v_cvt_pk_f16_f32 v81, v88, v89
	s_nop 0
	v_mfma_f32_16x16x32_f16 v[38:41], v[2:5], v[34:37], v[62:65]
	v_mfma_f32_16x16x32_f16 v[42:45], v[14:17], v[34:37], v[66:69]
	ds_read_b128 v[82:85], v94 offset:640
	ds_read_b128 v[86:89], v94 offset:656
	v_mfma_f32_16x16x32_f16 v[46:49], v[6:9], v[78:81], v[26:29]
	v_min_u32_e32 v1, v38, v40
	v_min_u32_e32 v0, v39, v41
	v_mfma_f32_16x16x32_f16 v[50:53], v[18:21], v[78:81], v[30:33]
	v_min3_u32 v1, v1, v42, v44
	v_min3_u32 v0, v0, v43, v45
	v_exp_f32_e32 v1, v1
	v_exp_f32_e32 v0, v0
	v_add_f32_e32 v1, 1.0, v1
	v_add_f32_e32 v0, 1.0, v0
	v_rcp_f32_e32 v1, v1
	v_rcp_f32_e32 v0, v0
	v_lshl_add_u64 v[92:93], v[90:91], 0, s[0:1]
	v_cvt_pk_f16_f32 v34, v1, v0
	v_lshl_add_u64 v[96:97], v[90:91], 0, s[2:3]
	v_lshl_add_u64 v[98:99], v[90:91], 0, s[4:5]
	v_mov_b32_dpp v35, v34 quad_perm:[1,2,3,0] row_mask:0xf bank_mask:0xf bound_ctrl:1
	v_mov_b32_dpp v36, v34 quad_perm:[2,3,0,1] row_mask:0xf bank_mask:0xf bound_ctrl:1
	v_mov_b32_dpp v37, v34 quad_perm:[3,0,1,2] row_mask:0xf bank_mask:0xf bound_ctrl:1
	v_lshl_add_u64 v[100:101], v[90:91], 0, s[6:7]
	s_nop 0
	v_mfma_f32_16x16x32_f16 v[38:41], v[2:5], v[34:37], v[70:73]
	v_mfma_f32_16x16x32_f16 v[42:45], v[14:17], v[34:37], v[74:77]
	s_waitcnt lgkmcnt(0)
	v_mfma_f32_16x16x32_f16 v[54:57], v[10:13], v[78:81], v[26:29]
	v_min_u32_e32 v1, v38, v40
	v_min_u32_e32 v0, v39, v41
	v_mfma_f32_16x16x32_f16 v[58:61], v[22:25], v[78:81], v[30:33]
	v_min3_u32 v1, v1, v42, v44
	v_min3_u32 v0, v0, v43, v45
	v_exp_f32_e32 v1, v1
	v_exp_f32_e32 v0, v0
	v_add_f32_e32 v1, 1.0, v1
	v_add_f32_e32 v0, 1.0, v0
	v_rcp_f32_e32 v1, v1
	v_rcp_f32_e32 v0, v0
	v_cvt_pk_f16_f32 v78, v82, v83
	v_cvt_pk_f16_f32 v34, v1, v0
	v_cvt_pk_f16_f32 v79, v84, v85
	v_cvt_pk_f16_f32 v80, v86, v87
	v_mov_b32_dpp v35, v34 quad_perm:[1,2,3,0] row_mask:0xf bank_mask:0xf bound_ctrl:1
	v_mov_b32_dpp v36, v34 quad_perm:[2,3,0,1] row_mask:0xf bank_mask:0xf bound_ctrl:1
	v_mov_b32_dpp v37, v34 quad_perm:[3,0,1,2] row_mask:0xf bank_mask:0xf bound_ctrl:1
	v_cvt_pk_f16_f32 v81, v88, v89
	s_nop 0
	v_mfma_f32_16x16x32_f16 v[38:41], v[2:5], v[34:37], v[46:49]
	v_mfma_f32_16x16x32_f16 v[42:45], v[14:17], v[34:37], v[50:53]
	ds_read_b128 v[82:85], v94 offset:768
	ds_read_b128 v[86:89], v94 offset:784
	v_mfma_f32_16x16x32_f16 v[62:65], v[6:9], v[78:81], v[26:29]
	v_min_u32_e32 v1, v38, v40
	v_min_u32_e32 v0, v39, v41
	v_mfma_f32_16x16x32_f16 v[66:69], v[18:21], v[78:81], v[30:33]
	v_min3_u32 v1, v1, v42, v44
	v_min3_u32 v0, v0, v43, v45
	v_exp_f32_e32 v1, v1
	v_exp_f32_e32 v0, v0
	v_add_f32_e32 v1, 1.0, v1
	v_add_f32_e32 v0, 1.0, v0
	v_rcp_f32_e32 v1, v1
	v_rcp_f32_e32 v0, v0
	s_nop 0
	v_cvt_pk_f16_f32 v34, v1, v0
	s_nop 0
	s_nop 0
	v_mov_b32_dpp v35, v34 quad_perm:[1,2,3,0] row_mask:0xf bank_mask:0xf bound_ctrl:1
	v_mov_b32_dpp v36, v34 quad_perm:[2,3,0,1] row_mask:0xf bank_mask:0xf bound_ctrl:1
	v_mov_b32_dpp v37, v34 quad_perm:[3,0,1,2] row_mask:0xf bank_mask:0xf bound_ctrl:1
	s_nop 0
	s_nop 0
	v_mfma_f32_16x16x32_f16 v[38:41], v[2:5], v[34:37], v[54:57]
	v_mfma_f32_16x16x32_f16 v[42:45], v[14:17], v[34:37], v[58:61]
	s_waitcnt lgkmcnt(0)
	v_mfma_f32_16x16x32_f16 v[70:73], v[10:13], v[78:81], v[26:29]
	v_min_u32_e32 v1, v38, v40
	v_min_u32_e32 v0, v39, v41
	v_mfma_f32_16x16x32_f16 v[74:77], v[22:25], v[78:81], v[30:33]
	v_min3_u32 v1, v1, v42, v44
	v_min3_u32 v0, v0, v43, v45
	v_exp_f32_e32 v1, v1
	v_exp_f32_e32 v0, v0
	v_add_f32_e32 v1, 1.0, v1
	v_add_f32_e32 v0, 1.0, v0
	v_rcp_f32_e32 v1, v1
	v_rcp_f32_e32 v0, v0
	v_cvt_pk_f16_f32 v78, v82, v83
	v_cvt_pk_f16_f32 v34, v1, v0
	v_cvt_pk_f16_f32 v79, v84, v85
	v_cvt_pk_f16_f32 v80, v86, v87
	v_mov_b32_dpp v35, v34 quad_perm:[1,2,3,0] row_mask:0xf bank_mask:0xf bound_ctrl:1
	v_mov_b32_dpp v36, v34 quad_perm:[2,3,0,1] row_mask:0xf bank_mask:0xf bound_ctrl:1
	v_mov_b32_dpp v37, v34 quad_perm:[3,0,1,2] row_mask:0xf bank_mask:0xf bound_ctrl:1
	v_cvt_pk_f16_f32 v81, v88, v89
	s_nop 0
	v_mfma_f32_16x16x32_f16 v[38:41], v[2:5], v[34:37], v[62:65]
	v_mfma_f32_16x16x32_f16 v[42:45], v[14:17], v[34:37], v[66:69]
	ds_read_b128 v[82:85], v94 offset:896
	ds_read_b128 v[86:89], v94 offset:912
	v_mfma_f32_16x16x32_f16 v[46:49], v[6:9], v[78:81], v[26:29]
	v_min_u32_e32 v1, v38, v40
	v_min_u32_e32 v0, v39, v41
	v_mfma_f32_16x16x32_f16 v[50:53], v[18:21], v[78:81], v[30:33]
	v_min3_u32 v1, v1, v42, v44
	v_min3_u32 v0, v0, v43, v45
	v_exp_f32_e32 v1, v1
	v_exp_f32_e32 v0, v0
	v_add_f32_e32 v1, 1.0, v1
	v_add_f32_e32 v0, 1.0, v0
	v_rcp_f32_e32 v1, v1
	v_rcp_f32_e32 v0, v0
	s_nop 0
	v_cvt_pk_f16_f32 v34, v1, v0
	s_nop 0
	s_nop 0
	v_mov_b32_dpp v35, v34 quad_perm:[1,2,3,0] row_mask:0xf bank_mask:0xf bound_ctrl:1
	v_mov_b32_dpp v36, v34 quad_perm:[2,3,0,1] row_mask:0xf bank_mask:0xf bound_ctrl:1
	v_mov_b32_dpp v37, v34 quad_perm:[3,0,1,2] row_mask:0xf bank_mask:0xf bound_ctrl:1
	s_nop 0
	s_nop 0
	v_mfma_f32_16x16x32_f16 v[38:41], v[2:5], v[34:37], v[70:73]
	s_waitcnt vmcnt(8)
	s_cbranch_vccz .Ltail_wait
.Ltail_back:
	s_mov_b32 m0, s9
	v_mfma_f32_16x16x32_f16 v[42:45], v[14:17], v[34:37], v[74:77]
	s_waitcnt lgkmcnt(0)
	v_mfma_f32_16x16x32_f16 v[54:57], v[10:13], v[78:81], v[26:29]
	v_min_u32_e32 v1, v38, v40
	v_min_u32_e32 v0, v39, v41
	v_mfma_f32_16x16x32_f16 v[58:61], v[22:25], v[78:81], v[30:33]
	v_min3_u32 v1, v1, v42, v44
	v_min3_u32 v0, v0, v43, v45
	v_exp_f32_e32 v1, v1
	v_exp_f32_e32 v0, v0
	v_add_f32_e32 v1, 1.0, v1
	v_add_f32_e32 v0, 1.0, v0
	v_rcp_f32_e32 v1, v1
	v_rcp_f32_e32 v0, v0
	v_cvt_pk_f16_f32 v78, v82, v83
	v_cvt_pk_f16_f32 v34, v1, v0
	v_cvt_pk_f16_f32 v79, v84, v85
	v_cvt_pk_f16_f32 v80, v86, v87
	v_mov_b32_dpp v35, v34 quad_perm:[1,2,3,0] row_mask:0xf bank_mask:0xf bound_ctrl:1
	v_mov_b32_dpp v36, v34 quad_perm:[2,3,0,1] row_mask:0xf bank_mask:0xf bound_ctrl:1
	v_mov_b32_dpp v37, v34 quad_perm:[3,0,1,2] row_mask:0xf bank_mask:0xf bound_ctrl:1
	v_cvt_pk_f16_f32 v81, v88, v89
	s_nop 0
	v_mfma_f32_16x16x32_f16 v[38:41], v[2:5], v[34:37], v[46:49]
	s_cbranch_vccz .Lskip_dma12
	global_load_lds_dwordx4 v[92:93], off nt
.Lskip_dma12:
	s_add_i32 m0, s9, 0x440
	v_mfma_f32_16x16x32_f16 v[42:45], v[14:17], v[34:37], v[50:53]
	ds_read_b128 v[82:85], v95
	ds_read_b128 v[86:89], v95 offset:16
	v_mfma_f32_16x16x32_f16 v[62:65], v[6:9], v[78:81], v[26:29]
	v_min_u32_e32 v1, v38, v40
	v_min_u32_e32 v0, v39, v41
	v_mfma_f32_16x16x32_f16 v[66:69], v[18:21], v[78:81], v[30:33]
	v_min3_u32 v1, v1, v42, v44
	v_min3_u32 v0, v0, v43, v45
	v_exp_f32_e32 v1, v1
	v_exp_f32_e32 v0, v0
	v_add_f32_e32 v1, 1.0, v1
	v_add_f32_e32 v0, 1.0, v0
	v_rcp_f32_e32 v1, v1
	v_rcp_f32_e32 v0, v0
	s_nop 0
	v_cvt_pk_f16_f32 v34, v1, v0
	s_nop 0
	s_nop 0
	v_mov_b32_dpp v35, v34 quad_perm:[1,2,3,0] row_mask:0xf bank_mask:0xf bound_ctrl:1
	v_mov_b32_dpp v36, v34 quad_perm:[2,3,0,1] row_mask:0xf bank_mask:0xf bound_ctrl:1
	v_mov_b32_dpp v37, v34 quad_perm:[3,0,1,2] row_mask:0xf bank_mask:0xf bound_ctrl:1
	s_nop 0
	s_nop 0
	v_mfma_f32_16x16x32_f16 v[38:41], v[2:5], v[34:37], v[54:57]
	s_cbranch_vccz .Lskip_dma13
	global_load_lds_dwordx4 v[96:97], off nt
.Lskip_dma13:
	s_add_i32 m0, s9, 0x880
	v_mfma_f32_16x16x32_f16 v[42:45], v[14:17], v[34:37], v[58:61]
	s_waitcnt lgkmcnt(0)
	v_mfma_f32_16x16x32_f16 v[70:73], v[10:13], v[78:81], v[26:29]
	v_min_u32_e32 v1, v38, v40
	v_min_u32_e32 v0, v39, v41
	v_mfma_f32_16x16x32_f16 v[74:77], v[22:25], v[78:81], v[30:33]
	v_min3_u32 v1, v1, v42, v44
	v_min3_u32 v0, v0, v43, v45
	v_exp_f32_e32 v1, v1
	v_exp_f32_e32 v0, v0
	v_add_f32_e32 v1, 1.0, v1
	v_add_f32_e32 v0, 1.0, v0
	v_rcp_f32_e32 v1, v1
	v_rcp_f32_e32 v0, v0
	v_cvt_pk_f16_f32 v78, v82, v83
	v_cvt_pk_f16_f32 v34, v1, v0
	v_cvt_pk_f16_f32 v79, v84, v85
	v_cvt_pk_f16_f32 v80, v86, v87
	v_mov_b32_dpp v35, v34 quad_perm:[1,2,3,0] row_mask:0xf bank_mask:0xf bound_ctrl:1
	v_mov_b32_dpp v36, v34 quad_perm:[2,3,0,1] row_mask:0xf bank_mask:0xf bound_ctrl:1
	v_mov_b32_dpp v37, v34 quad_perm:[3,0,1,2] row_mask:0xf bank_mask:0xf bound_ctrl:1
	v_cvt_pk_f16_f32 v81, v88, v89
	s_nop 0
	v_mfma_f32_16x16x32_f16 v[38:41], v[2:5], v[34:37], v[62:65]
	s_cbranch_vccz .Lskip_dma14
	global_load_lds_dwordx4 v[98:99], off nt
.Lskip_dma14:
	s_add_i32 m0, s9, 0xcc0
	v_mfma_f32_16x16x32_f16 v[42:45], v[14:17], v[34:37], v[66:69]
	ds_read_b128 v[82:85], v95 offset:128
	ds_read_b128 v[86:89], v95 offset:144
	v_mfma_f32_16x16x32_f16 v[46:49], v[6:9], v[78:81], v[26:29]
	v_min_u32_e32 v1, v38, v40
	v_min_u32_e32 v0, v39, v41
	v_mfma_f32_16x16x32_f16 v[50:53], v[18:21], v[78:81], v[30:33]
	v_min3_u32 v1, v1, v42, v44
	v_min3_u32 v0, v0, v43, v45
	v_exp_f32_e32 v1, v1
	v_exp_f32_e32 v0, v0
	v_add_f32_e32 v1, 1.0, v1
	v_add_f32_e32 v0, 1.0, v0
	v_rcp_f32_e32 v1, v1
	v_rcp_f32_e32 v0, v0
	v_mov_b32_e32 v94, v95
	v_cvt_pk_f16_f32 v34, v1, v0
	s_nop 0
	s_nop 0
	v_mov_b32_dpp v35, v34 quad_perm:[1,2,3,0] row_mask:0xf bank_mask:0xf bound_ctrl:1
	v_mov_b32_dpp v36, v34 quad_perm:[2,3,0,1] row_mask:0xf bank_mask:0xf bound_ctrl:1
	v_mov_b32_dpp v37, v34 quad_perm:[3,0,1,2] row_mask:0xf bank_mask:0xf bound_ctrl:1
	s_nop 0
	s_nop 0
	v_mfma_f32_16x16x32_f16 v[38:41], v[2:5], v[34:37], v[70:73]
	s_cbranch_vccz .Lskip_dma15
	global_load_lds_dwordx4 v[100:101], off nt
.Lskip_dma15:
	v_mfma_f32_16x16x32_f16 v[42:45], v[14:17], v[34:37], v[74:77]
	s_waitcnt lgkmcnt(0)
	v_mfma_f32_16x16x32_f16 v[54:57], v[10:13], v[78:81], v[26:29]
	v_min_u32_e32 v1, v38, v40
	v_min_u32_e32 v0, v39, v41
	v_mfma_f32_16x16x32_f16 v[58:61], v[22:25], v[78:81], v[30:33]
	v_min3_u32 v1, v1, v42, v44
	v_min3_u32 v0, v0, v43, v45
	v_exp_f32_e32 v1, v1
	v_exp_f32_e32 v0, v0
	v_add_f32_e32 v1, 1.0, v1
	v_add_f32_e32 v0, 1.0, v0
	v_rcp_f32_e32 v1, v1
	v_rcp_f32_e32 v0, v0
	v_cvt_pk_f16_f32 v78, v82, v83
	v_cvt_pk_f16_f32 v34, v1, v0
	v_cvt_pk_f16_f32 v79, v84, v85
	v_cvt_pk_f16_f32 v80, v86, v87
	v_mov_b32_dpp v35, v34 quad_perm:[1,2,3,0] row_mask:0xf bank_mask:0xf bound_ctrl:1
	v_mov_b32_dpp v36, v34 quad_perm:[2,3,0,1] row_mask:0xf bank_mask:0xf bound_ctrl:1
	v_mov_b32_dpp v37, v34 quad_perm:[3,0,1,2] row_mask:0xf bank_mask:0xf bound_ctrl:1
	v_cvt_pk_f16_f32 v81, v88, v89
	s_nop 0
	s_cmp_eq_u32 s8, 32
	s_cbranch_scc0 .Lchunk_loop
	s_branch .Lepilogue
